# mixer A dil-4 loop: L2 prefetch (8 dummy dword loads per tile, one tile beyond the two LDS stages), head waits vmcnt(24)/(16)/(0)
# baseline (speedup 1.0000x reference)
; #define LAS __attribute__((address_space(3)))
; #define BA_LOAD(kn, vn, kt_) do { const int kb_ = kb_first + 32 * (kt_); \
;         _Pragma("unroll") for (int ii = 0; ii < 4; ++ii) { const size_t row_ = (size_t)(res + dil * (kb_ + vr + 8 * ii)); \
;             kn[ii] = *(const v4u*)(Kb + row_ * kpitch + 8 * vc); vn[ii] = *(const v4u*)(Vb + row_ * vpitch + 8 * vc); } } while (0)
; #define BA_LOAD(kn, vn, kt_) do { const int kb_ = kb_first + 32 * (kt_); \
;         _Pragma("unroll") for (int ii = 0; ii < 4; ++ii) { const size_t row_ = (size_t)(res + dil * (kb_ + vr + 8 * ii)); \
;             kn[ii] = *(const v4u*)(Kb + row_ * kpitch + 8 * vc); vn[ii] = *(const v4u*)(Vb + row_ * vpitch + 8 * vc); } } while (0)
; __device__ __forceinline__ void band_branch_fast(f32x16& o0, f32x16& o1, f32x4& lsum, unsigned& orw, const bf16x8 (&qf)[4], ...
;     ...
;     if (kt_lo < kt_hi) BA_LOAD(kn, vn, kt_lo);
;     for (int kt = kt_lo; kt < kt_hi; ++kt) {
; #pragma unroll
;         for (int ii = 0; ii < 4; ++ii) { const int r_ = vr + 8 * ii; *(LAS v4u*)(kst + r_ * 128 + ((vc ^ (r_ & 7)) * 16)) = kn[ii]; *(LAS v4u*)(vst + r_ * 128 + vc * 16) = vn[ii]; }
;         if (kt + 1 < kt_hi) BA_LOAD(kn, vn, kt + 1);
; __device__ __forceinline__ void mixer_a_phase(const bf16* AQ, const bf16* AK, const bf16* AV  , bf16* O, float* ST, float* ML, const float* rel_bias, LAS unsigned char* lds, int G, int blk, int tid, int lane, int wave) {
;     ...
;                 band_branch_fast(o0, o1, lsum, orw, qf, Kb, 512, Vb, 512, 4, r & 3, 2048, 128 * a - 64, 8, tab + TA_LEN, -(128 * a + 4 * i5 + (r >> 2)) + 64 + TA_OFF + 8 * hh, vst, lane);
.Lmx_pre4:
	v_and_b32_e32 v58, 7, v1
	v_xor_b32_e32 v59, v58, v196
	v_sub_u32_e32 v58, v59, v58
	v_lshlrev_b32_e32 v64, 4, v58
	v_ashrrev_i32_e32 v65, 31, v64
	v_readlane_b32 s98, v254, 59
	v_lshl_add_u64 v[106:107], v[158:159], 0, v[64:65]
	v_mov_b64_e32 v[108:109], v[160:161]
	v_lshl_add_u64 v[110:111], v[162:163], 0, v[64:65]
	v_mov_b64_e32 v[112:113], v[164:165]
	v_lshl_add_u64 v[114:115], v[166:167], 0, v[64:65]
	v_mov_b64_e32 v[116:117], v[168:169]
	v_lshl_add_u64 v[118:119], v[170:171], 0, v[64:65]
	v_mov_b64_e32 v[120:121], v[172:173]
	s_lshl_b32 s98, s98, 14
	s_add_i32 s98, s98, 0x4000
	s_mov_b32 s99, 0
	s_add_i32 m0, s98, 0x1000
	s_nop 0
	global_load_lds_dwordx4 v[106:107], off
	s_add_i32 m0, s98, 0x0
	v_lshl_add_u64 v[106:107], v[106:107], 0, s[20:21]
	global_load_lds_dwordx4 v[108:109], off
	s_add_i32 m0, s98, 0x1400
	v_lshl_add_u64 v[108:109], v[108:109], 0, s[20:21]
	global_load_lds_dwordx4 v[110:111], off
	s_add_i32 m0, s98, 0x400
	v_lshl_add_u64 v[110:111], v[110:111], 0, s[20:21]
	global_load_lds_dwordx4 v[112:113], off
	s_add_i32 m0, s98, 0x1800
	v_lshl_add_u64 v[112:113], v[112:113], 0, s[20:21]
	global_load_lds_dwordx4 v[114:115], off
	s_add_i32 m0, s98, 0x800
	v_lshl_add_u64 v[114:115], v[114:115], 0, s[20:21]
	global_load_lds_dwordx4 v[116:117], off
	s_add_i32 m0, s98, 0x1c00
	v_lshl_add_u64 v[116:117], v[116:117], 0, s[20:21]
	global_load_lds_dwordx4 v[118:119], off
	s_add_i32 m0, s98, 0xc00
	v_lshl_add_u64 v[118:119], v[118:119], 0, s[20:21]
	global_load_lds_dwordx4 v[120:121], off
	v_lshl_add_u64 v[120:121], v[120:121], 0, s[20:21]
	s_add_i32 s0, s36, 1
	s_cmp_lt_u32 s0, s37
	s_cbranch_scc0 .Lmx3_p1a
	global_load_dword v122, v[106:107], off
	global_load_dword v122, v[108:109], off
	global_load_dword v122, v[110:111], off
	global_load_dword v122, v[112:113], off
	global_load_dword v122, v[114:115], off
	global_load_dword v122, v[116:117], off
	global_load_dword v122, v[118:119], off
	global_load_dword v122, v[120:121], off
	s_add_i32 m0, s98, 0x3000
	s_nop 0
	global_load_lds_dwordx4 v[106:107], off
	s_add_i32 m0, s98, 0x2000
	v_lshl_add_u64 v[106:107], v[106:107], 0, s[20:21]
	global_load_lds_dwordx4 v[108:109], off
	s_add_i32 m0, s98, 0x3400
	v_lshl_add_u64 v[108:109], v[108:109], 0, s[20:21]
	global_load_lds_dwordx4 v[110:111], off
	s_add_i32 m0, s98, 0x2400
	v_lshl_add_u64 v[110:111], v[110:111], 0, s[20:21]
	global_load_lds_dwordx4 v[112:113], off
	s_add_i32 m0, s98, 0x3800
	v_lshl_add_u64 v[112:113], v[112:113], 0, s[20:21]
	global_load_lds_dwordx4 v[114:115], off
	s_add_i32 m0, s98, 0x2800
	v_lshl_add_u64 v[114:115], v[114:115], 0, s[20:21]
	global_load_lds_dwordx4 v[116:117], off
	s_add_i32 m0, s98, 0x3c00
	v_lshl_add_u64 v[116:117], v[116:117], 0, s[20:21]
	global_load_lds_dwordx4 v[118:119], off
	s_add_i32 m0, s98, 0x2c00
	v_lshl_add_u64 v[118:119], v[118:119], 0, s[20:21]
	global_load_lds_dwordx4 v[120:121], off
	v_lshl_add_u64 v[120:121], v[120:121], 0, s[20:21]
	s_add_i32 s0, s36, 2
	s_cmp_lt_u32 s0, s37
	s_cbranch_scc0 .Lmx3_p1a
	global_load_dword v122, v[106:107], off
	global_load_dword v122, v[108:109], off
	global_load_dword v122, v[110:111], off
	global_load_dword v122, v[112:113], off
	global_load_dword v122, v[114:115], off
	global_load_dword v122, v[116:117], off
	global_load_dword v122, v[118:119], off
	global_load_dword v122, v[120:121], off

; #define LAS __attribute__((address_space(3)))
; #define BA_LOAD(kn, vn, kt_) do { const int kb_ = kb_first + 32 * (kt_); \
;         _Pragma("unroll") for (int ii = 0; ii < 4; ++ii) { const size_t row_ = (size_t)(res + dil * (kb_ + vr + 8 * ii)); \
;             kn[ii] = *(const v4u*)(Kb + row_ * kpitch + 8 * vc); vn[ii] = *(const v4u*)(Vb + row_ * vpitch + 8 * vc); } } while (0)
; #define BA_TR(off_) __builtin_bit_cast(s16x4, __builtin_amdgcn_ds_read_tr16_b64_v4i16((LAS v4i16_t*)(trb + (off_))))
; #define BA_LOAD(kn, vn, kt_) do { const int kb_ = kb_first + 32 * (kt_); \
;         _Pragma("unroll") for (int ii = 0; ii < 4; ++ii) { const size_t row_ = (size_t)(res + dil * (kb_ + vr + 8 * ii)); \
;             kn[ii] = *(const v4u*)(Kb + row_ * kpitch + 8 * vc); vn[ii] = *(const v4u*)(Vb + row_ * vpitch + 8 * vc); } } while (0)
; #define BA_TR(off_) __builtin_bit_cast(s16x4, __builtin_amdgcn_ds_read_tr16_b64_v4i16((LAS v4i16_t*)(trb + (off_))))
; #define BA_TR(off_) __builtin_bit_cast(s16x4, __builtin_amdgcn_ds_read_tr16_b64_v4i16((LAS v4i16_t*)(trb + (off_))))
; #define BA_TR(off_) __builtin_bit_cast(s16x4, __builtin_amdgcn_ds_read_tr16_b64_v4i16((LAS v4i16_t*)(trb + (off_))))
; __device__ __forceinline__ void band_branch_fast(f32x16& o0, f32x16& o1, f32x4& lsum, unsigned& orw, const bf16x8 (&qf)[4], ...
;     ...
;     for (int kt = kt_lo; kt < kt_hi; ++kt) {
; #pragma unroll
;         for (int ii = 0; ii < 4; ++ii) { const int r_ = vr + 8 * ii; *(LAS v4u*)(kst + r_ * 128 + ((vc ^ (r_ & 7)) * 16)) = kn[ii]; *(LAS v4u*)(vst + r_ * 128 + vc * 16) = vn[ii]; }
;         if (kt + 1 < kt_hi) BA_LOAD(kn, vn, kt + 1);
;         bf16x8 kf[4];
; #pragma unroll
;         for (int d0 = 0; d0 < 4; ++d0) kf[d0] = *(const LAS bf16x8*)(krd + (((2 * d0 + hh) ^ (pi & 7)) * 16));
;         const LAS float* tp = tab + (kb_first + 32 * kt + tboff);
;         f32x16 s;
; #pragma unroll
;         for (int r = 0; r < 16; ++r) s[r] = tp[(r & 7) + 16 * (r >> 3)];
;         s16x4 vt[8];
; #pragma unroll
;         for (int i = 0; i < 8; ++i) vt[i] = BA_TR((i >> 2) * 2048 + ((i >> 1) & 1) * 64 + (i & 1) * 512);
;         __builtin_amdgcn_sched_barrier(0);
; #pragma unroll
;         for (int d0 = 0; d0 < 4; ++d0) s = __builtin_amdgcn_mfma_f32_32x32x16_bf16(kf[d0], qf[d0], s, 0, 0, 0);
.LBB0_397:
	v_add3_u32 v38, v195, v200, s99
	v_add3_u32 v39, v195, v201, s99
	ds_read_b128 v[186:189], v38 offset:20480
	ds_read_b128 v[226:229], v39 offset:20480
	v_add3_u32 v38, v195, v202, s99
	v_add3_u32 v39, v195, v203, s99
	ds_read_b128 v[230:233], v38 offset:20480
	ds_read_b128 v[234:237], v39 offset:20480
	ds_read2_b32 v[38:39], v2 offset1:1
	ds_read2_b32 v[40:41], v2 offset0:2 offset1:3
	ds_read2_b32 v[42:43], v2 offset0:4 offset1:5
	ds_read2_b32 v[44:45], v2 offset0:6 offset1:7
	ds_read2_b32 v[46:47], v2 offset0:16 offset1:17
	ds_read2_b32 v[48:49], v2 offset0:18 offset1:19
	ds_read2_b32 v[50:51], v2 offset0:20 offset1:21
	ds_read2_b32 v[52:53], v2 offset0:22 offset1:23
	v_add3_u32 v137, v194, v193, s99
	ds_read_b64_tr_b16 v[238:239], v137 offset:16384
	ds_read_b64_tr_b16 v[240:241], v137 offset:16896
	ds_read_b64_tr_b16 v[244:245], v137 offset:16960
	ds_read_b64_tr_b16 v[242:243], v137 offset:16448
	ds_read_b64_tr_b16 v[246:247], v137 offset:18432
	ds_read_b64_tr_b16 v[248:249], v137 offset:18944
	ds_read_b64_tr_b16 v[252:253], v137 offset:19008
	ds_read_b64_tr_b16 v[250:251], v137 offset:18496
	s_waitcnt lgkmcnt(8)
	v_mfma_f32_32x32x16_bf16 v[38:53], v[186:189], v[74:77], v[38:53]
	v_mfma_f32_32x32x16_bf16 v[38:53], v[226:229], v[78:81], v[38:53]
	v_mfma_f32_32x32x16_bf16 v[38:53], v[230:233], v[82:85], v[38:53]
	v_mfma_f32_32x32x16_bf16 v[38:53], v[234:237], v[86:89], v[38:53]
	s_waitcnt lgkmcnt(0)
	s_add_i32 s0, s0, 1
	s_cmp_lt_u32 s0, s37
	s_cbranch_scc0 .Lmx3_skip
	s_add_i32 m0, s98, 0x1000
	s_nop 0
	global_load_lds_dwordx4 v[106:107], off
	s_add_i32 m0, s98, 0x0
	v_lshl_add_u64 v[106:107], v[106:107], 0, s[20:21]
	global_load_lds_dwordx4 v[108:109], off
	s_add_i32 m0, s98, 0x1400
	v_lshl_add_u64 v[108:109], v[108:109], 0, s[20:21]
	global_load_lds_dwordx4 v[110:111], off
	s_add_i32 m0, s98, 0x400
	v_lshl_add_u64 v[110:111], v[110:111], 0, s[20:21]
	global_load_lds_dwordx4 v[112:113], off
	s_add_i32 m0, s98, 0x1800
	v_lshl_add_u64 v[112:113], v[112:113], 0, s[20:21]
	global_load_lds_dwordx4 v[114:115], off
	s_add_i32 m0, s98, 0x800
	v_lshl_add_u64 v[114:115], v[114:115], 0, s[20:21]
	global_load_lds_dwordx4 v[116:117], off
	s_add_i32 m0, s98, 0x1c00
	v_lshl_add_u64 v[116:117], v[116:117], 0, s[20:21]
	global_load_lds_dwordx4 v[118:119], off
	s_add_i32 m0, s98, 0xc00
	v_lshl_add_u64 v[118:119], v[118:119], 0, s[20:21]
	global_load_lds_dwordx4 v[120:121], off
	v_lshl_add_u64 v[120:121], v[120:121], 0, s[20:21]
	s_add_i32 s100, s0, 1
	s_cmp_lt_u32 s100, s37
	s_cbranch_scc0 .Lmx3_skip
	global_load_dword v122, v[106:107], off
	global_load_dword v122, v[108:109], off
	global_load_dword v122, v[110:111], off
	global_load_dword v122, v[112:113], off
	global_load_dword v122, v[114:115], off
	global_load_dword v122, v[116:117], off
	global_load_dword v122, v[118:119], off
	global_load_dword v122, v[120:121], off

; #define LAS __attribute__((address_space(3)))
; #define BA_LOAD(kn, vn, kt_) do { const int kb_ = kb_first + 32 * (kt_); \
;         _Pragma("unroll") for (int ii = 0; ii < 4; ++ii) { const size_t row_ = (size_t)(res + dil * (kb_ + vr + 8 * ii)); \
;             kn[ii] = *(const v4u*)(Kb + row_ * kpitch + 8 * vc); vn[ii] = *(const v4u*)(Vb + row_ * vpitch + 8 * vc); } } while (0)
; #define BA_LOAD(kn, vn, kt_) do { const int kb_ = kb_first + 32 * (kt_); \
;         _Pragma("unroll") for (int ii = 0; ii < 4; ++ii) { const size_t row_ = (size_t)(res + dil * (kb_ + vr + 8 * ii)); \
;             kn[ii] = *(const v4u*)(Kb + row_ * kpitch + 8 * vc); vn[ii] = *(const v4u*)(Vb + row_ * vpitch + 8 * vc); } } while (0)
; __device__ __forceinline__ void band_branch_fast(f32x16& o0, f32x16& o1, f32x4& lsum, unsigned& orw, const bf16x8 (&qf)[4], ...
;     ...
;     for (int kt = kt_lo; kt < kt_hi; ++kt) {
; #pragma unroll
;         for (int ii = 0; ii < 4; ++ii) { const int r_ = vr + 8 * ii; *(LAS v4u*)(kst + r_ * 128 + ((vc ^ (r_ & 7)) * 16)) = kn[ii]; *(LAS v4u*)(vst + r_ * 128 + vc * 16) = vn[ii]; }
;         if (kt + 1 < kt_hi) BA_LOAD(kn, vn, kt + 1);
.LBB0_398:
	s_add_i32 s0, s0, 1
	s_cmp_ge_u32 s0, s37
	s_cselect_b64 s[10:11], -1, 0
	s_cbranch_scc1 .Lmx3_w0
	s_add_i32 s100, s0, 1
	s_cmp_ge_u32 s100, s37
	s_cbranch_scc1 .Lmx3_w16
	s_waitcnt vmcnt(24)
	s_branch .LBB0_397
.Lmx3_w16:
	s_waitcnt vmcnt(16)
	s_branch .LBB0_397
.Lmx3_w0:
	s_waitcnt vmcnt(0)
	s_branch .LBB0_397
